# flat->global in all GEMM/scan/combine/final regions; PP GEMM spread over all 256 WGs in dense-up phase
# speedup vs baseline: 1.0186x; 1.0109x over previous
; #define GAS __attribute__((address_space(1)))
; __device__ __forceinline__ unsigned pk2(float lo, float hi) { return f2bf(lo) | (f2bf(hi) << 16); }
; __device__ __forceinline__ void hgrn_scan(unsigned char* ws, int tid, int vcu, int G) {
;     const float* send = (const float*)(ws + WS_SEND); const float* dtot = (const float*)(ws + WS_DTOT); unsigned* sinit = (unsigned*)(ws + WS_SINIT);
;     for (int gid = vcu * (NWAVES * 64) + tid; gid < NB * HGH * 64 * 128; gid += G * NWAVES * 64) {
;         const int dp = gid & 63, e = (gid >> 6) & 127, bh = gid >> 13;
;         float s0 = 0.f, s1 = 0.f;
; #pragma unroll
;         for (int sc = 0; sc < HG_NSC - 1; ++sc) { const size_t item = (size_t)bh * HG_NSC + sc;
;             const f32x2 av = *(const GAS f32x2*)(send + (item * 128 + e) * 128 + 2 * dp), dv = *(const GAS f32x2*)(dtot + item * 128 + 2 * dp);
;             s0 = fmaf(dv.x, s0, av.x); s1 = fmaf(dv.y, s1, av.y);
;             sinit[((item + 1) * 128 + e) * 64 + dp] = pk2(s0, s1); }
;     }
; }
.LBB0_328:
	v_ashrrev_i32_e32 v8, 13, v10
	v_ashrrev_i32_e32 v9, 31, v8
	v_bfe_u32 v11, v10, 6, 7
	v_lshlrev_b64 v[6:7], 11, v[8:9]
	v_or_b32_e32 v12, v6, v11
	v_mov_b32_e32 v13, v7
	v_lshlrev_b64 v[12:13], 9, v[12:13]
	v_lshlrev_b64 v[8:9], 13, v[8:9]
	v_lshl_add_u64 v[12:13], v[0:1], 0, v[12:13]
	v_lshl_add_u64 v[8:9], v[2:3], 0, v[8:9]
	global_load_dwordx2 v[12:13], v[12:13], off
	v_or_b32_e32 v80, 0x80, v11
	global_load_dwordx2 v[14:15], v[8:9], off
	v_mov_b32_e32 v17, v7
	v_add_u32_e32 v10, s47, v10
	s_mov_b32 s0, 0x1ffff
	v_cmp_lt_i32_e32 vcc, s0, v10
	s_or_b64 s[4:5], vcc, s[4:5]
	s_waitcnt vmcnt(0)
	v_fma_f32 v12, 0, v14, v12
	v_fmac_f32_e32 v13, 0, v15
	v_bfe_u32 v14, v12, 16, 1
	v_add3_u32 v14, v12, v14, s95
	v_bfe_u32 v15, v13, 16, 1
	v_lshrrev_b32_e32 v14, 16, v14
	v_add3_u32 v15, v13, v15, s95
	v_and_or_b32 v16, v15, s94, v14
	v_or_b32_e32 v14, v80, v6
	v_mov_b32_e32 v15, v7
	v_lshlrev_b64 v[14:15], 8, v[14:15]
	v_lshl_add_u64 v[14:15], v[4:5], 0, v[14:15]
	global_store_dword v[14:15], v16, off
	v_or_b32_e32 v14, 0x80, v6
	v_or_b32_e32 v16, v14, v11
	v_lshlrev_b64 v[16:17], 9, v[16:17]
	v_lshl_add_u64 v[16:17], v[0:1], 0, v[16:17]
	global_load_dwordx2 v[16:17], v[16:17], off
	s_nop 0
	global_load_dwordx2 v[18:19], v[8:9], off offset:512
	v_mov_b32_e32 v15, v7
	s_waitcnt vmcnt(0)
	v_fma_f32 v16, v18, v12, v16
	v_fmac_f32_e32 v17, v19, v13
	v_bfe_u32 v12, v16, 16, 1
	v_add3_u32 v12, v16, v12, s95
	v_bfe_u32 v13, v17, 16, 1
	v_lshrrev_b32_e32 v12, 16, v12
	v_add3_u32 v13, v17, v13, s95
	v_and_or_b32 v18, v13, s94, v12
	v_lshl_add_u64 v[12:13], v[14:15], 0, v[80:81]
	v_lshlrev_b64 v[12:13], 8, v[12:13]
	v_lshl_add_u64 v[12:13], v[4:5], 0, v[12:13]
	global_store_dword v[12:13], v18, off
	v_or_b32_e32 v18, 0x100, v6
	v_or_b32_e32 v12, v18, v11
	v_mov_b32_e32 v13, v7
	v_lshlrev_b64 v[12:13], 9, v[12:13]
	v_lshl_add_u64 v[12:13], v[0:1], 0, v[12:13]
	global_load_dwordx2 v[12:13], v[12:13], off
	s_nop 0
	global_load_dwordx2 v[14:15], v[8:9], off offset:1024
	s_waitcnt vmcnt(0)
	v_fma_f32 v12, v14, v16, v12
	v_fmac_f32_e32 v13, v15, v17
	v_bfe_u32 v14, v12, 16, 1
	v_add3_u32 v14, v12, v14, s95
	v_bfe_u32 v15, v13, 16, 1
	v_lshrrev_b32_e32 v14, 16, v14
	v_add3_u32 v15, v13, v15, s95
	v_and_or_b32 v16, v15, s94, v14
	v_or_b32_e32 v14, v18, v80
	v_mov_b32_e32 v15, v7
	v_lshlrev_b64 v[14:15], 8, v[14:15]
	v_lshl_add_u64 v[14:15], v[4:5], 0, v[14:15]
	global_store_dword v[14:15], v16, off
	v_or_b32_e32 v14, 0x180, v6
	v_or_b32_e32 v16, v14, v11
	v_mov_b32_e32 v17, v7
	v_lshlrev_b64 v[16:17], 9, v[16:17]
	v_lshl_add_u64 v[16:17], v[0:1], 0, v[16:17]
	global_load_dwordx2 v[16:17], v[16:17], off
	s_nop 0
	global_load_dwordx2 v[18:19], v[8:9], off offset:1536
	v_mov_b32_e32 v15, v7
	s_waitcnt vmcnt(0)
	v_fma_f32 v16, v18, v12, v16
	v_fmac_f32_e32 v17, v19, v13
	v_bfe_u32 v12, v16, 16, 1
	v_add3_u32 v12, v16, v12, s95
	v_bfe_u32 v13, v17, 16, 1
	v_lshrrev_b32_e32 v12, 16, v12
	v_add3_u32 v13, v17, v13, s95
	v_and_or_b32 v18, v13, s94, v12
	v_lshl_add_u64 v[12:13], v[14:15], 0, v[80:81]
	v_lshlrev_b64 v[12:13], 8, v[12:13]
	v_lshl_add_u64 v[12:13], v[4:5], 0, v[12:13]
	global_store_dword v[12:13], v18, off
	v_or_b32_e32 v18, 0x200, v6
	v_or_b32_e32 v12, v18, v11
	v_mov_b32_e32 v13, v7
	v_lshlrev_b64 v[12:13], 9, v[12:13]
	v_lshl_add_u64 v[12:13], v[0:1], 0, v[12:13]
	global_load_dwordx2 v[12:13], v[12:13], off
	s_nop 0
	global_load_dwordx2 v[14:15], v[8:9], off offset:2048
	s_waitcnt vmcnt(0)
	v_fma_f32 v12, v14, v16, v12
	v_fmac_f32_e32 v13, v15, v17
	v_bfe_u32 v14, v12, 16, 1
	v_add3_u32 v14, v12, v14, s95
	v_bfe_u32 v15, v13, 16, 1
	v_lshrrev_b32_e32 v14, 16, v14
	v_add3_u32 v15, v13, v15, s95
	v_and_or_b32 v16, v15, s94, v14
	v_or_b32_e32 v14, v18, v80
	v_mov_b32_e32 v15, v7
	v_lshlrev_b64 v[14:15], 8, v[14:15]
	v_lshl_add_u64 v[14:15], v[4:5], 0, v[14:15]
	global_store_dword v[14:15], v16, off
	v_or_b32_e32 v14, 0x280, v6
	v_or_b32_e32 v16, v14, v11
	v_mov_b32_e32 v17, v7
	v_lshlrev_b64 v[16:17], 9, v[16:17]
	v_lshl_add_u64 v[16:17], v[0:1], 0, v[16:17]
	global_load_dwordx2 v[16:17], v[16:17], off
	s_nop 0
	global_load_dwordx2 v[18:19], v[8:9], off offset:2560
	v_mov_b32_e32 v15, v7
	s_waitcnt vmcnt(0)
	v_fma_f32 v16, v18, v12, v16
	v_fmac_f32_e32 v17, v19, v13
	v_bfe_u32 v12, v16, 16, 1
	v_add3_u32 v12, v16, v12, s95
	v_bfe_u32 v13, v17, 16, 1
	v_lshrrev_b32_e32 v12, 16, v12
	v_add3_u32 v13, v17, v13, s95
	v_and_or_b32 v18, v13, s94, v12
	v_lshl_add_u64 v[12:13], v[14:15], 0, v[80:81]
	v_lshlrev_b64 v[12:13], 8, v[12:13]
	v_lshl_add_u64 v[12:13], v[4:5], 0, v[12:13]
	global_store_dword v[12:13], v18, off
	v_or_b32_e32 v18, 0x300, v6
	v_or_b32_e32 v12, v18, v11
	v_mov_b32_e32 v13, v7
	v_lshlrev_b64 v[12:13], 9, v[12:13]
	v_lshl_add_u64 v[12:13], v[0:1], 0, v[12:13]
	global_load_dwordx2 v[12:13], v[12:13], off
	s_nop 0
	global_load_dwordx2 v[14:15], v[8:9], off offset:3072
	s_waitcnt vmcnt(0)
	v_fma_f32 v12, v14, v16, v12
	v_fmac_f32_e32 v13, v15, v17
	v_bfe_u32 v14, v12, 16, 1
	v_add3_u32 v14, v12, v14, s95
	v_bfe_u32 v15, v13, 16, 1
	v_lshrrev_b32_e32 v14, 16, v14
	v_add3_u32 v15, v13, v15, s95
	v_and_or_b32 v16, v15, s94, v14
	v_or_b32_e32 v14, v18, v80
	v_mov_b32_e32 v15, v7
	v_lshlrev_b64 v[14:15], 8, v[14:15]
	v_lshl_add_u64 v[14:15], v[4:5], 0, v[14:15]
	global_store_dword v[14:15], v16, off
	v_or_b32_e32 v14, 0x380, v6
	v_or_b32_e32 v16, v14, v11
	v_mov_b32_e32 v17, v7
	v_lshlrev_b64 v[16:17], 9, v[16:17]
	v_lshl_add_u64 v[16:17], v[0:1], 0, v[16:17]
	global_load_dwordx2 v[16:17], v[16:17], off
	s_nop 0
	global_load_dwordx2 v[8:9], v[8:9], off offset:3584
	v_mov_b32_e32 v15, v7
	s_waitcnt vmcnt(0)
; #define GAS __attribute__((address_space(1)))
; __device__ __forceinline__ unsigned pk2(float lo, float hi) { return f2bf(lo) | (f2bf(hi) << 16); }
; __device__ __forceinline__ void hgrn_scan(unsigned char* ws, int tid, int vcu, int G) {
;     const float* send = (const float*)(ws + WS_SEND); const float* dtot = (const float*)(ws + WS_DTOT); unsigned* sinit = (unsigned*)(ws + WS_SINIT);
;     for (int gid = vcu * (NWAVES * 64) + tid; gid < NB * HGH * 64 * 128; gid += G * NWAVES * 64) {
;         const int dp = gid & 63, e = (gid >> 6) & 127, bh = gid >> 13;
;         float s0 = 0.f, s1 = 0.f;
; #pragma unroll
;         for (int sc = 0; sc < HG_NSC - 1; ++sc) { const size_t item = (size_t)bh * HG_NSC + sc;
;             const f32x2 av = *(const GAS f32x2*)(send + (item * 128 + e) * 128 + 2 * dp), dv = *(const GAS f32x2*)(dtot + item * 128 + 2 * dp);
;             s0 = fmaf(dv.x, s0, av.x); s1 = fmaf(dv.y, s1, av.y);
;             sinit[((item + 1) * 128 + e) * 64 + dp] = pk2(s0, s1); }
;     }
; }
	v_fma_f32 v16, v8, v12, v16
	v_fmac_f32_e32 v17, v9, v13
	v_bfe_u32 v8, v16, 16, 1
	v_add3_u32 v8, v16, v8, s95
	v_bfe_u32 v9, v17, 16, 1
	v_lshrrev_b32_e32 v8, 16, v8
	v_add3_u32 v9, v17, v9, s95
	v_and_or_b32 v12, v9, s94, v8
	v_lshl_add_u64 v[8:9], v[14:15], 0, v[80:81]
	v_lshlrev_b64 v[8:9], 8, v[8:9]
	v_lshl_add_u64 v[8:9], v[4:5], 0, v[8:9]
	global_store_dword v[8:9], v12, off
	v_or_b32_e32 v8, 0x400, v6
	v_or_b32_e32 v12, v8, v11
	v_mov_b32_e32 v13, v7
	v_mov_b32_e32 v9, v7
	v_lshlrev_b64 v[12:13], 9, v[12:13]
	v_lshl_add_u64 v[12:13], v[0:1], 0, v[12:13]
	v_lshl_add_u64 v[14:15], v[8:9], 2, v[2:3]
	global_load_dwordx2 v[12:13], v[12:13], off
	v_or_b32_e32 v8, v8, v80
	global_load_dwordx2 v[14:15], v[14:15], off
	s_waitcnt vmcnt(0)
	v_fma_f32 v12, v14, v16, v12
	v_fmac_f32_e32 v13, v15, v17
	v_bfe_u32 v9, v12, 16, 1
	v_add3_u32 v9, v12, v9, s95
	v_bfe_u32 v14, v13, 16, 1
	v_lshrrev_b32_e32 v9, 16, v9
	v_add3_u32 v14, v13, v14, s95
	v_and_or_b32 v14, v14, s94, v9
	v_mov_b32_e32 v9, v7
	v_lshlrev_b64 v[8:9], 8, v[8:9]
	v_lshl_add_u64 v[8:9], v[4:5], 0, v[8:9]
	global_store_dword v[8:9], v14, off
	v_or_b32_e32 v8, 0x480, v6
	v_or_b32_e32 v14, v8, v11
	v_mov_b32_e32 v15, v7
	v_mov_b32_e32 v9, v7
	v_lshlrev_b64 v[14:15], 9, v[14:15]
	v_lshl_add_u64 v[14:15], v[0:1], 0, v[14:15]
	v_lshl_add_u64 v[16:17], v[8:9], 2, v[2:3]
	global_load_dwordx2 v[14:15], v[14:15], off
	v_lshl_add_u64 v[8:9], v[8:9], 0, v[80:81]
	global_load_dwordx2 v[16:17], v[16:17], off
	v_lshlrev_b64 v[8:9], 8, v[8:9]
	v_lshl_add_u64 v[8:9], v[4:5], 0, v[8:9]
	s_waitcnt vmcnt(0)
	v_fma_f32 v14, v16, v12, v14
	v_fmac_f32_e32 v15, v17, v13
	v_bfe_u32 v12, v14, 16, 1
	v_add3_u32 v12, v14, v12, s95
	v_bfe_u32 v13, v15, 16, 1
	v_lshrrev_b32_e32 v12, 16, v12
	v_add3_u32 v13, v15, v13, s95
	v_and_or_b32 v12, v13, s94, v12
	global_store_dword v[8:9], v12, off
	v_or_b32_e32 v8, 0x500, v6
	v_or_b32_e32 v12, v8, v11
	v_mov_b32_e32 v13, v7
	v_mov_b32_e32 v9, v7
	v_lshlrev_b64 v[12:13], 9, v[12:13]
	v_lshl_add_u64 v[12:13], v[0:1], 0, v[12:13]
	v_lshl_add_u64 v[16:17], v[8:9], 2, v[2:3]
	global_load_dwordx2 v[12:13], v[12:13], off
	v_or_b32_e32 v8, v8, v80
	global_load_dwordx2 v[16:17], v[16:17], off
	s_waitcnt vmcnt(0)
	v_fma_f32 v12, v16, v14, v12
	v_fmac_f32_e32 v13, v17, v15
	v_bfe_u32 v9, v12, 16, 1
	v_add3_u32 v9, v12, v9, s95
	v_bfe_u32 v14, v13, 16, 1
	v_lshrrev_b32_e32 v9, 16, v9
	v_add3_u32 v14, v13, v14, s95
	v_and_or_b32 v14, v14, s94, v9
	v_mov_b32_e32 v9, v7
	v_lshlrev_b64 v[8:9], 8, v[8:9]
	v_lshl_add_u64 v[8:9], v[4:5], 0, v[8:9]
	global_store_dword v[8:9], v14, off
	v_or_b32_e32 v8, 0x580, v6
	v_or_b32_e32 v14, v8, v11
	v_mov_b32_e32 v15, v7
	v_mov_b32_e32 v9, v7
	v_lshlrev_b64 v[14:15], 9, v[14:15]
	v_lshl_add_u64 v[14:15], v[0:1], 0, v[14:15]
	v_lshl_add_u64 v[16:17], v[8:9], 2, v[2:3]
	global_load_dwordx2 v[14:15], v[14:15], off
	v_lshl_add_u64 v[8:9], v[8:9], 0, v[80:81]
	global_load_dwordx2 v[16:17], v[16:17], off
	v_lshlrev_b64 v[8:9], 8, v[8:9]
	v_lshl_add_u64 v[8:9], v[4:5], 0, v[8:9]
	s_waitcnt vmcnt(0)
	v_fma_f32 v14, v16, v12, v14
	v_fmac_f32_e32 v15, v17, v13
	v_bfe_u32 v12, v14, 16, 1
	v_add3_u32 v12, v14, v12, s95
	v_bfe_u32 v13, v15, 16, 1
	v_lshrrev_b32_e32 v12, 16, v12
	v_add3_u32 v13, v15, v13, s95
	v_and_or_b32 v12, v13, s94, v12
	global_store_dword v[8:9], v12, off
	v_or_b32_e32 v8, 0x600, v6
	v_or_b32_e32 v12, v8, v11
	v_mov_b32_e32 v13, v7
	v_mov_b32_e32 v9, v7
	v_lshlrev_b64 v[12:13], 9, v[12:13]
	v_lshl_add_u64 v[12:13], v[0:1], 0, v[12:13]
	v_lshl_add_u64 v[16:17], v[8:9], 2, v[2:3]
	global_load_dwordx2 v[12:13], v[12:13], off
	v_or_b32_e32 v8, v8, v80
	global_load_dwordx2 v[16:17], v[16:17], off
	s_waitcnt vmcnt(0)
	v_fma_f32 v12, v16, v14, v12
	v_fmac_f32_e32 v13, v17, v15
	v_bfe_u32 v9, v12, 16, 1
	v_add3_u32 v9, v12, v9, s95
	v_bfe_u32 v14, v13, 16, 1
	v_lshrrev_b32_e32 v9, 16, v9
	v_add3_u32 v14, v13, v14, s95
	v_and_or_b32 v14, v14, s94, v9
	v_mov_b32_e32 v9, v7
	v_lshlrev_b64 v[8:9], 8, v[8:9]
	v_lshl_add_u64 v[8:9], v[4:5], 0, v[8:9]
	global_store_dword v[8:9], v14, off
	v_or_b32_e32 v8, 0x680, v6
	v_or_b32_e32 v14, v8, v11
	v_mov_b32_e32 v15, v7
	v_mov_b32_e32 v9, v7
	v_lshlrev_b64 v[14:15], 9, v[14:15]
	v_lshl_add_u64 v[14:15], v[0:1], 0, v[14:15]
	v_lshl_add_u64 v[16:17], v[8:9], 2, v[2:3]
	global_load_dwordx2 v[14:15], v[14:15], off
	v_lshl_add_u64 v[8:9], v[8:9], 0, v[80:81]
	global_load_dwordx2 v[16:17], v[16:17], off
	v_lshlrev_b64 v[8:9], 8, v[8:9]
	v_lshl_add_u64 v[8:9], v[4:5], 0, v[8:9]
	v_or_b32_e32 v6, 0x700, v6
	s_waitcnt vmcnt(0)
	v_fma_f32 v14, v16, v12, v14
	v_fmac_f32_e32 v15, v17, v13
	v_bfe_u32 v12, v14, 16, 1
	v_add3_u32 v12, v14, v12, s95
	v_bfe_u32 v13, v15, 16, 1
	v_lshrrev_b32_e32 v12, 16, v12
	v_add3_u32 v13, v15, v13, s95
	v_and_or_b32 v12, v13, s94, v12
	global_store_dword v[8:9], v12, off
	v_or_b32_e32 v8, v6, v11
	v_mov_b32_e32 v9, v7
	v_lshlrev_b64 v[8:9], 9, v[8:9]
	v_lshl_add_u64 v[8:9], v[0:1], 0, v[8:9]
	v_lshl_add_u64 v[12:13], v[6:7], 2, v[2:3]
	global_load_dwordx2 v[8:9], v[8:9], off
	v_or_b32_e32 v6, v6, v80
	global_load_dwordx2 v[12:13], v[12:13], off
	v_lshlrev_b64 v[6:7], 8, v[6:7]
	v_lshl_add_u64 v[6:7], v[4:5], 0, v[6:7]
	s_waitcnt vmcnt(0)
	v_fma_f32 v8, v12, v14, v8
	v_fmac_f32_e32 v9, v13, v15
	v_bfe_u32 v11, v8, 16, 1
	v_add3_u32 v8, v8, v11, s95
	v_bfe_u32 v11, v9, 16, 1
	v_lshrrev_b32_e32 v8, 16, v8
	v_add3_u32 v9, v9, v11, s95
	v_and_or_b32 v8, v9, s94, v8
	global_store_dword v[6:7], v8, off
	s_andn2_b64 exec, exec, s[4:5]
	s_cbranch_execnz .LBB0_328

; __device__ __forceinline__ int ld_agent_i(const int* p) { return (int)__hip_atomic_load((const unsigned*)p, RLX_AGENT); }
; #define OPQ_LANE() int z_ = 0; asm volatile("" : "+v"(z_)); const int ln = (int)__builtin_amdgcn_mbcnt_hi(~0u, __builtin_amdgcn_mbcnt_lo(~0u, (unsigned)z_)); const int tidv = F.wave * 64 + ln; (void)tidv; int bix = blockIdx.x; asm volatile("" : "+s"(bix)); (void)bix
; __global__ void __launch_bounds__(NWAVES * 64, 2) mk_fwd(Args args) {
;     ...
;         if (IN(pb + P_CMB)) {
;             if (l & 1) {
;                 OPQ_LANE();
;                 const bf16* Y = (const bf16*)(ws + WS_Y); const int* posg = (const int*)(ws + WS_TBL + T_POS);
;                 int gwo = gw; asm volatile("" : "+s"(gwo));
;                 const int pr = gwo + (ln & 7) * NGW; const int p1v = ld_agent_i(posg + 2 * pr), p2v = ld_agent_i(posg + 2 * pr + 1);
;                 for (int k0 = 0; k0 < M / NGW; k0 += 4) {
.LBB0_1186:
	v_readlane_b32 s4, v255, 43
	v_readlane_b32 s5, v255, 44
	s_cmp_gt_i32 s4, s18
	s_cselect_b64 s[0:1], -1, 0
	s_cmp_ge_i32 s18, s5
	s_cselect_b64 s[2:3], -1, 0
	s_or_b64 s[0:1], s[0:1], s[2:3]
	v_readlane_b32 s2, v255, 47
	v_readlane_b32 s3, v255, 48
	s_or_b64 s[0:1], s[2:3], s[0:1]
	s_and_b64 vcc, exec, s[0:1]
	v_readlane_b32 s68, v255, 40
	v_readlane_b32 s51, v255, 35
	v_readlane_b32 s69, v255, 41
	s_cbranch_vccnz .LBB0_1252
	v_mov_b32_e32 v0, v81
	v_readlane_b32 s0, v254, 2
	v_mbcnt_lo_u32_b32 v0, -1, v0
	v_mbcnt_hi_u32_b32 v2, -1, v0
	v_and_b32_e32 v0, 7, v2
	s_mov_b32 s4, s60
	v_mul_lo_u32 v0, v0, s54
	s_mov_b64 s[0:1], 0x238000
	v_add_lshl_u32 v0, s4, v0, 1
	s_waitcnt lgkmcnt(0)
	v_ashrrev_i32_e32 v1, 31, v0
	v_lshl_add_u64 v[0:1], v[0:1], 2, s[80:81]
	v_lshl_add_u64 v[4:5], v[0:1], 0, s[0:1]
	v_add_co_u32_e32 v0, vcc, 0x238000, v0
	v_readlane_b32 s0, v255, 23
	s_nop 0
	v_addc_co_u32_e32 v1, vcc, 0, v1, vcc
	s_waitcnt vmcnt(0)
	global_load_dword v80, v[0:1], off sc1
	global_load_dword v110, v[4:5], off offset:4 sc1
	v_readlane_b32 s1, v255, 24
	s_andn2_b64 vcc, exec, s[0:1]
	s_cbranch_vccnz .LBB0_1198
	v_ashrrev_i32_e32 v3, 31, v2
	v_lshlrev_b32_e32 v0, 2, v2
	s_add_u32 s12, s80, 0x19a00000
	v_xor_b32_e32 v111, 4, v0
	v_xor_b32_e32 v112, 8, v0
	v_xor_b32_e32 v113, 16, v0
	v_xor_b32_e32 v114, 32, v0
	v_xor_b32_e32 v115, 64, v0
	v_xor_b32_e32 v116, 0x80, v0
	v_lshl_add_u64 v[0:1], v[2:3], 2, s[80:81]
	s_mov_b64 s[0:1], 0x300000
	s_addc_u32 s13, s81, 0
	v_cmp_gt_i32_e32 vcc, 16, v2
	v_lshl_add_u64 v[0:1], v[0:1], 0, s[0:1]
	s_mov_b32 s0, 0
	v_cmp_eq_u32_e64 s[2:3], 0, v2
	v_lshlrev_b64 v[2:3], 3, v[2:3]
	s_branch .LBB0_1190

; __device__ __forceinline__ float bf_lo(unsigned u) { return __uint_as_float(u << 16); }
; __device__ __forceinline__ float bf_hi(unsigned u) { return __uint_as_float(u & 0xffff0000u); }
; __device__ __forceinline__ float f16_lo(unsigned u) { return (float)__builtin_bit_cast(h16x2, u)[0]; }
; __device__ __forceinline__ float f16_hi(unsigned u) { return (float)__builtin_bit_cast(h16x2, u)[1]; }
; #define GAS __attribute__((address_space(1)))
; __global__ void __launch_bounds__(NWAVES * 64, 2) mk_fwd(Args args) {
;     ...
;                 for (int k0 = 0; k0 < M / NGW; k0 += 4) {
;                     v2u hv[4][4], ya[4][4], yb[4][4];
; #pragma unroll
;                     for (int r = 0; r < 4; ++r) { const int p1 = __builtin_amdgcn_readlane(p1v, k0 + r), p2 = __builtin_amdgcn_readlane(p2v, k0 + r);
;                         const GAS v2u* xr = (const GAS v2u*)(hy + (size_t)(gwo + (k0 + r) * NGW) * D) + ln;
;                         const GAS v2u* y1 = (const GAS v2u*)(Y + (size_t)p1 * D) + ln; const GAS v2u* y2 = (const GAS v2u*)(Y + (size_t)p2 * D) + ln;
; #pragma unroll
;                         for (int q = 0; q < 4; ++q) { hv[r][q] = xr[64 * q]; ya[r][q] = y1[64 * q]; yb[r][q] = y2[64 * q]; } }
; #pragma unroll
;                     for (int r = 0; r < 4; ++r) { const int mr = gwo + (k0 + r) * NGW; float ss = 0.f; f32x4 v[4];
; #pragma unroll
;                         for (int q = 0; q < 4; ++q) { const v2u h = hv[r][q], a = ya[r][q], b = yb[r][q];
;                             v[q].x = pg8::f16_lo(h.x) + (pg8::bf_lo(a.x) + pg8::bf_lo(b.x)); v[q].y = pg8::f16_hi(h.x) + (pg8::bf_hi(a.x) + pg8::bf_hi(b.x));
;                             v[q].z = pg8::f16_lo(h.y) + (pg8::bf_lo(a.y) + pg8::bf_lo(b.y)); v[q].w = pg8::f16_hi(h.y) + (pg8::bf_hi(a.y) + pg8::bf_hi(b.y));
;                             ss += (v[q].x * v[q].x + v[q].y * v[q].y) + (v[q].z * v[q].z + v[q].w * v[q].w); }
.LBB0_1190:
	s_ashr_i32 s5, s4, 31
	s_lshl_b64 s[10:11], s[4:5], 11
	s_waitcnt vmcnt(0) lgkmcnt(0)
	v_readlane_b32 s6, v80, s0
	s_add_u32 s10, s72, s10
	s_addc_u32 s11, s73, s11
	s_ashr_i32 s7, s6, 31
	s_lshl_b64 s[6:7], s[6:7], 11
	v_readlane_b32 s8, v110, s0
	s_add_u32 s6, s12, s6
	s_addc_u32 s7, s13, s7
	s_ashr_i32 s9, s8, 31
	v_lshl_add_u64 v[4:5], s[6:7], 0, v[2:3]
	s_lshl_b64 s[6:7], s[8:9], 11
	s_add_u32 s6, s12, s6
	v_lshl_add_u64 v[70:71], s[10:11], 0, v[2:3]
	s_addc_u32 s7, s13, s7
	v_lshl_add_u64 v[6:7], s[6:7], 0, v[2:3]
	global_load_dwordx2 v[108:109], v[70:71], off
	global_load_dwordx2 v[106:107], v[4:5], off
	global_load_dwordx2 v[104:105], v[6:7], off
	global_load_dwordx2 v[102:103], v[70:71], off offset:512
	global_load_dwordx2 v[100:101], v[4:5], off offset:512
	global_load_dwordx2 v[98:99], v[6:7], off offset:512
	global_load_dwordx2 v[96:97], v[70:71], off offset:1024
	global_load_dwordx2 v[94:95], v[4:5], off offset:1024
	global_load_dwordx2 v[92:93], v[6:7], off offset:1024
	global_load_dwordx2 v[86:87], v[70:71], off offset:1536
	global_load_dwordx2 v[88:89], v[4:5], off offset:1536
	global_load_dwordx2 v[90:91], v[6:7], off offset:1536
	s_add_i32 s10, s54, s4
	s_ashr_i32 s11, s10, 31
	s_add_i32 s1, s0, 1
	s_lshl_b64 s[14:15], s[10:11], 11
	v_readlane_b32 s6, v80, s1
	s_add_u32 s14, s72, s14
	s_addc_u32 s15, s73, s15
	s_ashr_i32 s7, s6, 31
	s_lshl_b64 s[6:7], s[6:7], 11
	v_readlane_b32 s8, v110, s1
	s_add_u32 s6, s12, s6
	s_addc_u32 s7, s13, s7
	s_ashr_i32 s9, s8, 31
	v_lshl_add_u64 v[4:5], s[6:7], 0, v[2:3]
	s_lshl_b64 s[6:7], s[8:9], 11
	s_add_u32 s6, s12, s6
	s_addc_u32 s7, s13, s7
	s_add_i32 s8, s74, s4
	s_ashr_i32 s9, s8, 31
	s_add_i32 s1, s0, 2
	s_lshl_b64 s[16:17], s[8:9], 11
	v_lshl_add_u64 v[6:7], s[6:7], 0, v[2:3]
	v_readlane_b32 s6, v80, s1
	s_add_u32 s16, s72, s16
	s_addc_u32 s17, s73, s17
	s_ashr_i32 s7, s6, 31
	s_lshl_b64 s[6:7], s[6:7], 11
	v_lshl_add_u64 v[44:45], s[14:15], 0, v[2:3]
	v_readlane_b32 s14, v110, s1
	s_add_u32 s6, s12, s6
	s_addc_u32 s7, s13, s7
	s_ashr_i32 s15, s14, 31
	global_load_dwordx2 v[84:85], v[44:45], off
	global_load_dwordx2 v[82:83], v[4:5], off
	global_load_dwordx2 v[78:79], v[6:7], off
	global_load_dwordx2 v[76:77], v[44:45], off offset:512
	global_load_dwordx2 v[74:75], v[4:5], off offset:512
	global_load_dwordx2 v[72:73], v[6:7], off offset:512
	global_load_dwordx2 v[68:69], v[44:45], off offset:1024
	global_load_dwordx2 v[66:67], v[4:5], off offset:1024
	global_load_dwordx2 v[64:65], v[6:7], off offset:1024
	global_load_dwordx2 v[58:59], v[44:45], off offset:1536
	global_load_dwordx2 v[60:61], v[4:5], off offset:1536
	global_load_dwordx2 v[62:63], v[6:7], off offset:1536
	v_lshl_add_u64 v[4:5], s[6:7], 0, v[2:3]
	s_lshl_b64 s[6:7], s[14:15], 11
	s_add_u32 s6, s12, s6
	s_addc_u32 s7, s13, s7
	v_lshl_add_u64 v[6:7], s[6:7], 0, v[2:3]
	s_add_i32 s6, s53, s4
	s_ashr_i32 s7, s6, 31
	s_add_i32 s14, s0, 3
	s_lshl_b64 s[18:19], s[6:7], 11
	v_readlane_b32 s0, v80, s14
	s_add_u32 s18, s72, s18
	s_addc_u32 s19, s73, s19
	s_ashr_i32 s1, s0, 31
	s_lshl_b64 s[0:1], s[0:1], 11
	v_lshl_add_u64 v[18:19], s[16:17], 0, v[2:3]
	v_readlane_b32 s16, v110, s14
	s_add_u32 s0, s12, s0
	s_addc_u32 s1, s13, s1
	s_ashr_i32 s17, s16, 31
	v_lshl_add_u64 v[8:9], s[0:1], 0, v[2:3]
	s_lshl_b64 s[0:1], s[16:17], 11
	s_add_u32 s0, s12, s0
	s_addc_u32 s1, s13, s1
	global_load_dwordx2 v[56:57], v[18:19], off
	global_load_dwordx2 v[54:55], v[4:5], off
	global_load_dwordx2 v[52:53], v[6:7], off
	global_load_dwordx2 v[50:51], v[18:19], off offset:512
	global_load_dwordx2 v[48:49], v[4:5], off offset:512
	global_load_dwordx2 v[46:47], v[6:7], off offset:512
	global_load_dwordx2 v[42:43], v[18:19], off offset:1024
	global_load_dwordx2 v[40:41], v[4:5], off offset:1024
	global_load_dwordx2 v[38:39], v[6:7], off offset:1024
	global_load_dwordx2 v[32:33], v[18:19], off offset:1536
	global_load_dwordx2 v[34:35], v[4:5], off offset:1536
	global_load_dwordx2 v[36:37], v[6:7], off offset:1536
	v_lshl_add_u64 v[4:5], s[18:19], 0, v[2:3]
	v_lshl_add_u64 v[10:11], s[0:1], 0, v[2:3]
	global_load_dwordx2 v[30:31], v[4:5], off
	global_load_dwordx2 v[28:29], v[8:9], off
	global_load_dwordx2 v[26:27], v[10:11], off
	global_load_dwordx2 v[24:25], v[4:5], off offset:512
	global_load_dwordx2 v[22:23], v[8:9], off offset:512
	global_load_dwordx2 v[20:21], v[10:11], off offset:512
	global_load_dwordx2 v[16:17], v[4:5], off offset:1024
	global_load_dwordx2 v[14:15], v[8:9], off offset:1024
	global_load_dwordx2 v[12:13], v[10:11], off offset:1024
	global_load_dwordx2 v[6:7], v[4:5], off offset:1536
	s_nop 0
	global_load_dwordx2 v[8:9], v[8:9], off offset:1536
	s_nop 0
	global_load_dwordx2 v[10:11], v[10:11], off offset:1536
	s_waitcnt vmcnt(47)
	v_cvt_f32_f16_e32 v118, v108
	v_cvt_f32_f16_sdwa v119, v108 dst_sel:DWORD dst_unused:UNUSED_PAD src0_sel:WORD_1
	s_waitcnt vmcnt(46)
	v_lshlrev_b32_e32 v120, 16, v106
	v_and_b32_e32 v121, 0xffff0000, v106
	s_waitcnt vmcnt(45)
	v_lshlrev_b32_e32 v122, 16, v104
	v_and_b32_e32 v123, 0xffff0000, v104
	v_pk_add_f32 v[120:121], v[120:121], v[122:123]
	v_cvt_f32_f16_e32 v108, v109
	v_cvt_f32_f16_sdwa v109, v109 dst_sel:DWORD dst_unused:UNUSED_PAD src0_sel:WORD_1
	v_pk_add_f32 v[118:119], v[120:121], v[118:119]
	v_lshlrev_b32_e32 v106, 16, v107
	v_pk_mul_f32 v[120:121], v[118:119], v[118:119]
	v_cvt_pk_f16_f32 v104, v118, v119
	v_and_b32_e32 v107, 0xffff0000, v107
	v_lshlrev_b32_e32 v118, 16, v105
	v_and_b32_e32 v119, 0xffff0000, v105
	v_pk_add_f32 v[106:107], v[106:107], v[118:119]
	s_waitcnt vmcnt(42)
; __device__ __forceinline__ float bf_lo(unsigned u) { return __uint_as_float(u << 16); }
; __device__ __forceinline__ float bf_hi(unsigned u) { return __uint_as_float(u & 0xffff0000u); }
; __device__ __forceinline__ float f16_lo(unsigned u) { return (float)__builtin_bit_cast(h16x2, u)[0]; }
; __device__ __forceinline__ float f16_hi(unsigned u) { return (float)__builtin_bit_cast(h16x2, u)[1]; }
; #define GAS __attribute__((address_space(1)))
; __device__ __forceinline__ float wave_sum(float v, int lane) {
; #pragma unroll
;     for (int o = 1; o < 64; o <<= 1) v += __builtin_bit_cast(float, __builtin_amdgcn_ds_bpermute((lane ^ o) << 2, __builtin_bit_cast(int, v)));
;     return v;
; __global__ void __launch_bounds__(NWAVES * 64, 2) mk_fwd(Args args) {
;     ...
;                     for (int r = 0; r < 4; ++r) { const int mr = gwo + (k0 + r) * NGW; float ss = 0.f; f32x4 v[4];
; #pragma unroll
;                         for (int q = 0; q < 4; ++q) { const v2u h = hv[r][q], a = ya[r][q], b = yb[r][q];
;                             v[q].x = pg8::f16_lo(h.x) + (pg8::bf_lo(a.x) + pg8::bf_lo(b.x)); v[q].y = pg8::f16_hi(h.x) + (pg8::bf_hi(a.x) + pg8::bf_hi(b.x));
;                             v[q].z = pg8::f16_lo(h.y) + (pg8::bf_lo(a.y) + pg8::bf_lo(b.y)); v[q].w = pg8::f16_hi(h.y) + (pg8::bf_hi(a.y) + pg8::bf_hi(b.y));
;                             ss += (v[q].x * v[q].x + v[q].y * v[q].y) + (v[q].z * v[q].z + v[q].w * v[q].w); }
;                         ss = wave_sum(ss, ln);
;                         GAS v2u* o8 = (GAS v2u*)(ub + (size_t)mr * D) + ln;
; #pragma unroll
;                         for (int q = 0; q < 4; ++q) { v2u w; w.x = pg8::pk_f16(v[q].x, v[q].y); w.y = pg8::pk_f16(v[q].z, v[q].w); o8[64 * q] = w; }
;                         if (ln < 16) ((float*)(ws + WS_TBL + T_SSP))[(size_t)mr * 16 + ln] = (ln == 0) ? ss : 0.f; }
	v_lshlrev_b32_e32 v118, 16, v98
	v_pk_add_f32 v[106:107], v[106:107], v[108:109]
	v_and_b32_e32 v119, 0xffff0000, v98
	v_cvt_pk_f16_f32 v105, v106, v107
	global_store_dwordx2 v[70:71], v[104:105], off
	v_cvt_f32_f16_e32 v104, v102
	v_cvt_f32_f16_sdwa v105, v102 dst_sel:DWORD dst_unused:UNUSED_PAD src0_sel:WORD_1
	v_pk_mul_f32 v[108:109], v[106:107], v[106:107]
	v_lshlrev_b32_e32 v106, 16, v100
	v_and_b32_e32 v107, 0xffff0000, v100
	v_pk_add_f32 v[106:107], v[106:107], v[118:119]
	v_cvt_f32_f16_e32 v102, v103
	v_cvt_f32_f16_sdwa v103, v103 dst_sel:DWORD dst_unused:UNUSED_PAD src0_sel:WORD_1
	v_pk_add_f32 v[104:105], v[106:107], v[104:105]
	v_lshlrev_b32_e32 v100, 16, v101
	v_pk_mul_f32 v[106:107], v[104:105], v[104:105]
	v_cvt_pk_f16_f32 v98, v104, v105
	v_and_b32_e32 v101, 0xffff0000, v101
	v_lshlrev_b32_e32 v104, 16, v99
	v_and_b32_e32 v105, 0xffff0000, v99
	v_pk_add_f32 v[100:101], v[100:101], v[104:105]
	s_waitcnt vmcnt(40)
	v_lshlrev_b32_e32 v104, 16, v92
	v_pk_add_f32 v[100:101], v[100:101], v[102:103]
	v_and_b32_e32 v105, 0xffff0000, v92
	v_cvt_pk_f16_f32 v99, v100, v101
	global_store_dwordx2 v[70:71], v[98:99], off offset:512
	v_cvt_f32_f16_e32 v98, v96
	v_cvt_f32_f16_sdwa v99, v96 dst_sel:DWORD dst_unused:UNUSED_PAD src0_sel:WORD_1
	v_pk_mul_f32 v[102:103], v[100:101], v[100:101]
	v_lshlrev_b32_e32 v100, 16, v94
	v_and_b32_e32 v101, 0xffff0000, v94
	v_pk_add_f32 v[100:101], v[100:101], v[104:105]
	v_cvt_f32_f16_e32 v96, v97
	v_cvt_f32_f16_sdwa v97, v97 dst_sel:DWORD dst_unused:UNUSED_PAD src0_sel:WORD_1
	v_pk_add_f32 v[98:99], v[100:101], v[98:99]
	v_lshlrev_b32_e32 v94, 16, v95
	v_pk_mul_f32 v[100:101], v[98:99], v[98:99]
	v_cvt_pk_f16_f32 v92, v98, v99
	v_and_b32_e32 v95, 0xffff0000, v95
	v_lshlrev_b32_e32 v98, 16, v93
	v_and_b32_e32 v99, 0xffff0000, v93
	v_pk_add_f32 v[94:95], v[94:95], v[98:99]
	s_waitcnt vmcnt(38)
	v_lshlrev_b32_e32 v98, 16, v90
	v_pk_add_f32 v[94:95], v[94:95], v[96:97]
	v_and_b32_e32 v99, 0xffff0000, v90
	v_cvt_pk_f16_f32 v93, v94, v95
	global_store_dwordx2 v[70:71], v[92:93], off offset:1024
	v_cvt_f32_f16_e32 v92, v86
	v_cvt_f32_f16_sdwa v93, v86 dst_sel:DWORD dst_unused:UNUSED_PAD src0_sel:WORD_1
	v_pk_mul_f32 v[96:97], v[94:95], v[94:95]
	v_lshlrev_b32_e32 v94, 16, v88
	v_and_b32_e32 v95, 0xffff0000, v88
	v_pk_add_f32 v[94:95], v[94:95], v[98:99]
	v_cvt_f32_f16_e32 v86, v87
	v_pk_add_f32 v[92:93], v[94:95], v[92:93]
	v_cvt_f32_f16_sdwa v87, v87 dst_sel:DWORD dst_unused:UNUSED_PAD src0_sel:WORD_1
	v_pk_mul_f32 v[94:95], v[92:93], v[92:93]
	v_cvt_pk_f16_f32 v88, v92, v93
	v_lshlrev_b32_e32 v92, 16, v89
	v_and_b32_e32 v93, 0xffff0000, v89
	v_lshlrev_b32_e32 v90, 16, v91
	v_and_b32_e32 v91, 0xffff0000, v91
	v_pk_add_f32 v[90:91], v[92:93], v[90:91]
	v_add_f32_e32 v89, v102, v103
	v_add_f32_e32 v92, v106, v107
	v_add_f32_e32 v89, v89, v92
	v_add_f32_e32 v92, v108, v109
	v_add_f32_e32 v93, v120, v121
	v_pk_add_f32 v[90:91], v[90:91], v[86:87]
	v_add_f32_e32 v92, v92, v93
	v_pk_mul_f32 v[86:87], v[90:91], v[90:91]
	v_add_f32_e32 v89, v92, v89
	v_add_f32_e32 v92, v96, v97
	v_add_f32_e32 v93, v100, v101
	v_add_f32_e32 v92, v92, v93
	v_add_f32_e32 v86, v86, v87
	v_add_f32_e32 v87, v94, v95
	v_add_f32_e32 v89, v89, v92
	v_add_f32_e32 v86, v86, v87
	v_add_f32_e32 v86, v89, v86
	ds_bpermute_b32 v87, v111, v86
	v_cvt_pk_f16_f32 v89, v90, v91
	global_store_dwordx2 v[70:71], v[88:89], off offset:1536
	s_waitcnt lgkmcnt(0)
	v_add_f32_e32 v86, v86, v87
	ds_bpermute_b32 v87, v112, v86
	s_waitcnt lgkmcnt(0)
	v_add_f32_e32 v86, v86, v87
	ds_bpermute_b32 v87, v113, v86
	s_waitcnt lgkmcnt(0)
	v_add_f32_e32 v86, v86, v87
	ds_bpermute_b32 v87, v114, v86
	s_waitcnt lgkmcnt(0)
	v_add_f32_e32 v86, v86, v87
	ds_bpermute_b32 v87, v115, v86
	s_waitcnt lgkmcnt(0)
	v_add_f32_e32 v86, v86, v87
	ds_bpermute_b32 v87, v116, v86
	s_and_saveexec_b64 s[0:1], vcc
	s_cbranch_execz .LBB0_1192
	s_waitcnt lgkmcnt(0)
	v_add_f32_e32 v86, v86, v87
	s_lshl_b64 s[16:17], s[4:5], 6
	v_lshl_add_u64 v[70:71], v[0:1], 0, s[16:17]
	v_cndmask_b32_e64 v86, 0, v86, s[2:3]
	global_store_dword v[70:71], v86, off
.LBB0_1192:
	s_or_b64 exec, exec, s[0:1]
	s_waitcnt vmcnt(0)
	v_lshlrev_b32_e32 v86, 16, v82
	s_waitcnt lgkmcnt(0)
	v_and_b32_e32 v87, 0xffff0000, v82
	v_lshlrev_b32_e32 v88, 16, v78
	v_and_b32_e32 v89, 0xffff0000, v78
	v_cvt_f32_f16_sdwa v71, v84 dst_sel:DWORD dst_unused:UNUSED_PAD src0_sel:WORD_1
	v_cvt_f32_f16_e32 v70, v84
	v_pk_add_f32 v[86:87], v[86:87], v[88:89]
	v_cvt_f32_f16_sdwa v89, v85 dst_sel:DWORD dst_unused:UNUSED_PAD src0_sel:WORD_1
	v_cvt_f32_f16_e32 v88, v85
	v_lshlrev_b32_e32 v82, 16, v83
	v_and_b32_e32 v83, 0xffff0000, v83
	v_lshlrev_b32_e32 v78, 16, v79
	v_and_b32_e32 v79, 0xffff0000, v79
	v_pk_add_f32 v[78:79], v[82:83], v[78:79]
	v_pk_add_f32 v[70:71], v[86:87], v[70:71]
	v_pk_add_f32 v[78:79], v[78:79], v[88:89]
	v_pk_mul_f32 v[86:87], v[70:71], v[70:71]
	v_cvt_pk_f16_f32 v70, v70, v71
	v_pk_mul_f32 v[82:83], v[78:79], v[78:79]
	v_cvt_pk_f16_f32 v71, v78, v79
	v_lshlrev_b32_e32 v78, 16, v74
	v_and_b32_e32 v79, 0xffff0000, v74
	v_lshlrev_b32_e32 v84, 16, v72
	v_and_b32_e32 v85, 0xffff0000, v72
	global_store_dwordx2 v[44:45], v[70:71], off
	v_cvt_f32_f16_sdwa v71, v76 dst_sel:DWORD dst_unused:UNUSED_PAD src0_sel:WORD_1
	v_cvt_f32_f16_e32 v70, v76
	v_pk_add_f32 v[78:79], v[78:79], v[84:85]
	v_cvt_f32_f16_sdwa v85, v77 dst_sel:DWORD dst_unused:UNUSED_PAD src0_sel:WORD_1
	v_cvt_f32_f16_e32 v84, v77
	v_lshlrev_b32_e32 v74, 16, v75
	v_and_b32_e32 v75, 0xffff0000, v75
	v_lshlrev_b32_e32 v72, 16, v73
	v_and_b32_e32 v73, 0xffff0000, v73
	v_pk_add_f32 v[72:73], v[74:75], v[72:73]
	v_pk_add_f32 v[70:71], v[78:79], v[70:71]
; __device__ __forceinline__ float bf_lo(unsigned u) { return __uint_as_float(u << 16); }
; __device__ __forceinline__ float bf_hi(unsigned u) { return __uint_as_float(u & 0xffff0000u); }
; __device__ __forceinline__ float f16_lo(unsigned u) { return (float)__builtin_bit_cast(h16x2, u)[0]; }
; __device__ __forceinline__ float f16_hi(unsigned u) { return (float)__builtin_bit_cast(h16x2, u)[1]; }
; #define GAS __attribute__((address_space(1)))
; __device__ __forceinline__ float wave_sum(float v, int lane) {
; #pragma unroll
;     for (int o = 1; o < 64; o <<= 1) v += __builtin_bit_cast(float, __builtin_amdgcn_ds_bpermute((lane ^ o) << 2, __builtin_bit_cast(int, v)));
;     return v;
; __global__ void __launch_bounds__(NWAVES * 64, 2) mk_fwd(Args args) {
;     ...
;                     for (int r = 0; r < 4; ++r) { const int mr = gwo + (k0 + r) * NGW; float ss = 0.f; f32x4 v[4];
; #pragma unroll
;                         for (int q = 0; q < 4; ++q) { const v2u h = hv[r][q], a = ya[r][q], b = yb[r][q];
;                             v[q].x = pg8::f16_lo(h.x) + (pg8::bf_lo(a.x) + pg8::bf_lo(b.x)); v[q].y = pg8::f16_hi(h.x) + (pg8::bf_hi(a.x) + pg8::bf_hi(b.x));
;                             v[q].z = pg8::f16_lo(h.y) + (pg8::bf_lo(a.y) + pg8::bf_lo(b.y)); v[q].w = pg8::f16_hi(h.y) + (pg8::bf_hi(a.y) + pg8::bf_hi(b.y));
;                             ss += (v[q].x * v[q].x + v[q].y * v[q].y) + (v[q].z * v[q].z + v[q].w * v[q].w); }
;                         ss = wave_sum(ss, ln);
;                         GAS v2u* o8 = (GAS v2u*)(ub + (size_t)mr * D) + ln;
; #pragma unroll
;                         for (int q = 0; q < 4; ++q) { v2u w; w.x = pg8::pk_f16(v[q].x, v[q].y); w.y = pg8::pk_f16(v[q].z, v[q].w); o8[64 * q] = w; }
;                         if (ln < 16) ((float*)(ws + WS_TBL + T_SSP))[(size_t)mr * 16 + ln] = (ln == 0) ? ss : 0.f; }
	v_pk_add_f32 v[72:73], v[72:73], v[84:85]
	v_pk_mul_f32 v[78:79], v[70:71], v[70:71]
	v_cvt_pk_f16_f32 v70, v70, v71
	v_cvt_pk_f16_f32 v71, v72, v73
	global_store_dwordx2 v[44:45], v[70:71], off offset:512
	v_cvt_f32_f16_sdwa v71, v68 dst_sel:DWORD dst_unused:UNUSED_PAD src0_sel:WORD_1
	v_cvt_f32_f16_e32 v70, v68
	v_pk_mul_f32 v[74:75], v[72:73], v[72:73]
	v_lshlrev_b32_e32 v72, 16, v66
	v_and_b32_e32 v73, 0xffff0000, v66
	v_lshlrev_b32_e32 v76, 16, v64
	v_and_b32_e32 v77, 0xffff0000, v64
	v_pk_add_f32 v[72:73], v[72:73], v[76:77]
	v_lshlrev_b32_e32 v66, 16, v67
	v_pk_add_f32 v[70:71], v[72:73], v[70:71]
	v_and_b32_e32 v67, 0xffff0000, v67
	v_pk_mul_f32 v[72:73], v[70:71], v[70:71]
	v_cvt_pk_f16_f32 v64, v70, v71
	v_cvt_f32_f16_sdwa v71, v69 dst_sel:DWORD dst_unused:UNUSED_PAD src0_sel:WORD_1
	v_cvt_f32_f16_e32 v70, v69
	v_lshlrev_b32_e32 v68, 16, v65
	v_and_b32_e32 v69, 0xffff0000, v65
	v_pk_add_f32 v[66:67], v[66:67], v[68:69]
	s_nop 0
	v_pk_add_f32 v[66:67], v[66:67], v[70:71]
	v_lshlrev_b32_e32 v70, 16, v62
	v_cvt_pk_f16_f32 v65, v66, v67
	global_store_dwordx2 v[44:45], v[64:65], off offset:1024
	v_cvt_f32_f16_sdwa v65, v58 dst_sel:DWORD dst_unused:UNUSED_PAD src0_sel:WORD_1
	v_cvt_f32_f16_e32 v64, v58
	v_pk_mul_f32 v[68:69], v[66:67], v[66:67]
	v_lshlrev_b32_e32 v66, 16, v60
	v_and_b32_e32 v67, 0xffff0000, v60
	v_and_b32_e32 v71, 0xffff0000, v62
	v_pk_add_f32 v[66:67], v[66:67], v[70:71]
	v_lshlrev_b32_e32 v58, 16, v61
	v_pk_add_f32 v[64:65], v[66:67], v[64:65]
	v_lshlrev_b32_e32 v62, 16, v63
	v_pk_mul_f32 v[66:67], v[64:65], v[64:65]
	v_cvt_pk_f16_f32 v60, v64, v65
	v_cvt_f32_f16_sdwa v65, v59 dst_sel:DWORD dst_unused:UNUSED_PAD src0_sel:WORD_1
	v_cvt_f32_f16_e32 v64, v59
	v_and_b32_e32 v59, 0xffff0000, v61
	v_and_b32_e32 v63, 0xffff0000, v63
	v_pk_add_f32 v[58:59], v[58:59], v[62:63]
	v_add_f32_e32 v61, v74, v75
	v_pk_add_f32 v[62:63], v[58:59], v[64:65]
	v_add_f32_e32 v64, v78, v79
	v_add_f32_e32 v61, v61, v64
	v_add_f32_e32 v64, v82, v83
	v_add_f32_e32 v65, v86, v87
	v_add_f32_e32 v64, v64, v65
	v_pk_mul_f32 v[58:59], v[62:63], v[62:63]
	v_add_f32_e32 v61, v64, v61
	v_add_f32_e32 v64, v68, v69
	v_add_f32_e32 v65, v72, v73
	v_add_f32_e32 v64, v64, v65
	v_add_f32_e32 v58, v58, v59
	v_add_f32_e32 v59, v66, v67
	v_add_f32_e32 v61, v61, v64
	v_add_f32_e32 v58, v58, v59
	v_add_f32_e32 v58, v61, v58
	ds_bpermute_b32 v59, v111, v58
	v_cvt_pk_f16_f32 v61, v62, v63
	global_store_dwordx2 v[44:45], v[60:61], off offset:1536
	s_waitcnt lgkmcnt(0)
	v_add_f32_e32 v58, v58, v59
	ds_bpermute_b32 v59, v112, v58
	s_waitcnt lgkmcnt(0)
	v_add_f32_e32 v58, v58, v59
	ds_bpermute_b32 v59, v113, v58
	s_waitcnt lgkmcnt(0)
	v_add_f32_e32 v58, v58, v59
	ds_bpermute_b32 v59, v114, v58
	s_waitcnt lgkmcnt(0)
	v_add_f32_e32 v58, v58, v59
	ds_bpermute_b32 v59, v115, v58
	s_waitcnt lgkmcnt(0)
	v_add_f32_e32 v58, v58, v59
	ds_bpermute_b32 v59, v116, v58
	s_and_saveexec_b64 s[0:1], vcc
	s_cbranch_execz .LBB0_1194
	s_waitcnt lgkmcnt(0)
	v_add_f32_e32 v58, v58, v59
	s_lshl_b64 s[10:11], s[10:11], 6
	v_lshl_add_u64 v[44:45], v[0:1], 0, s[10:11]
	v_cndmask_b32_e64 v58, 0, v58, s[2:3]
	global_store_dword v[44:45], v58, off
.LBB0_1194:
	s_or_b64 exec, exec, s[0:1]
	v_lshlrev_b32_e32 v58, 16, v54
	s_waitcnt lgkmcnt(0)
	v_and_b32_e32 v59, 0xffff0000, v54
	v_lshlrev_b32_e32 v60, 16, v52
	v_and_b32_e32 v61, 0xffff0000, v52
	v_cvt_f32_f16_sdwa v45, v56 dst_sel:DWORD dst_unused:UNUSED_PAD src0_sel:WORD_1
	v_cvt_f32_f16_e32 v44, v56
	v_pk_add_f32 v[58:59], v[58:59], v[60:61]
	v_cvt_f32_f16_sdwa v61, v57 dst_sel:DWORD dst_unused:UNUSED_PAD src0_sel:WORD_1
	v_cvt_f32_f16_e32 v60, v57
	v_lshlrev_b32_e32 v54, 16, v55
	v_and_b32_e32 v55, 0xffff0000, v55
	v_lshlrev_b32_e32 v52, 16, v53
	v_and_b32_e32 v53, 0xffff0000, v53
	v_pk_add_f32 v[52:53], v[54:55], v[52:53]
	v_pk_add_f32 v[44:45], v[58:59], v[44:45]
	v_pk_add_f32 v[52:53], v[52:53], v[60:61]
	v_pk_mul_f32 v[58:59], v[44:45], v[44:45]
	v_cvt_pk_f16_f32 v44, v44, v45
	v_pk_mul_f32 v[54:55], v[52:53], v[52:53]
	v_cvt_pk_f16_f32 v45, v52, v53
	v_lshlrev_b32_e32 v52, 16, v48
	v_and_b32_e32 v53, 0xffff0000, v48
	v_lshlrev_b32_e32 v56, 16, v46
	v_and_b32_e32 v57, 0xffff0000, v46
	global_store_dwordx2 v[18:19], v[44:45], off
	v_cvt_f32_f16_sdwa v45, v50 dst_sel:DWORD dst_unused:UNUSED_PAD src0_sel:WORD_1
	v_cvt_f32_f16_e32 v44, v50
	v_pk_add_f32 v[52:53], v[52:53], v[56:57]
	v_cvt_f32_f16_sdwa v57, v51 dst_sel:DWORD dst_unused:UNUSED_PAD src0_sel:WORD_1
	v_cvt_f32_f16_e32 v56, v51
	v_lshlrev_b32_e32 v48, 16, v49
	v_and_b32_e32 v49, 0xffff0000, v49
	v_lshlrev_b32_e32 v46, 16, v47
	v_and_b32_e32 v47, 0xffff0000, v47
	v_pk_add_f32 v[46:47], v[48:49], v[46:47]
	v_pk_add_f32 v[44:45], v[52:53], v[44:45]
	v_pk_add_f32 v[46:47], v[46:47], v[56:57]
	v_pk_mul_f32 v[52:53], v[44:45], v[44:45]
	v_cvt_pk_f16_f32 v44, v44, v45
	v_cvt_pk_f16_f32 v45, v46, v47
	global_store_dwordx2 v[18:19], v[44:45], off offset:512
	v_cvt_f32_f16_sdwa v45, v42 dst_sel:DWORD dst_unused:UNUSED_PAD src0_sel:WORD_1
	v_cvt_f32_f16_e32 v44, v42
	v_pk_mul_f32 v[48:49], v[46:47], v[46:47]
	v_lshlrev_b32_e32 v46, 16, v40
	v_and_b32_e32 v47, 0xffff0000, v40
	v_lshlrev_b32_e32 v50, 16, v38
	v_and_b32_e32 v51, 0xffff0000, v38
	v_pk_add_f32 v[46:47], v[46:47], v[50:51]
	v_lshlrev_b32_e32 v40, 16, v41
	v_pk_add_f32 v[44:45], v[46:47], v[44:45]
	v_and_b32_e32 v41, 0xffff0000, v41
	v_pk_mul_f32 v[46:47], v[44:45], v[44:45]
	v_cvt_pk_f16_f32 v38, v44, v45
	v_cvt_f32_f16_sdwa v45, v43 dst_sel:DWORD dst_unused:UNUSED_PAD src0_sel:WORD_1
	v_cvt_f32_f16_e32 v44, v43
	v_lshlrev_b32_e32 v42, 16, v39
	v_and_b32_e32 v43, 0xffff0000, v39
	v_pk_add_f32 v[40:41], v[40:41], v[42:43]
	s_nop 0
; __device__ __forceinline__ float bf_lo(unsigned u) { return __uint_as_float(u << 16); }
; __device__ __forceinline__ float bf_hi(unsigned u) { return __uint_as_float(u & 0xffff0000u); }
; __device__ __forceinline__ float f16_lo(unsigned u) { return (float)__builtin_bit_cast(h16x2, u)[0]; }
; __device__ __forceinline__ float f16_hi(unsigned u) { return (float)__builtin_bit_cast(h16x2, u)[1]; }
; #define GAS __attribute__((address_space(1)))
; __device__ __forceinline__ float wave_sum(float v, int lane) {
; #pragma unroll
;     for (int o = 1; o < 64; o <<= 1) v += __builtin_bit_cast(float, __builtin_amdgcn_ds_bpermute((lane ^ o) << 2, __builtin_bit_cast(int, v)));
;     return v;
; __global__ void __launch_bounds__(NWAVES * 64, 2) mk_fwd(Args args) {
;     ...
;                     for (int r = 0; r < 4; ++r) { const int mr = gwo + (k0 + r) * NGW; float ss = 0.f; f32x4 v[4];
; #pragma unroll
;                         for (int q = 0; q < 4; ++q) { const v2u h = hv[r][q], a = ya[r][q], b = yb[r][q];
;                             v[q].x = pg8::f16_lo(h.x) + (pg8::bf_lo(a.x) + pg8::bf_lo(b.x)); v[q].y = pg8::f16_hi(h.x) + (pg8::bf_hi(a.x) + pg8::bf_hi(b.x));
;                             v[q].z = pg8::f16_lo(h.y) + (pg8::bf_lo(a.y) + pg8::bf_lo(b.y)); v[q].w = pg8::f16_hi(h.y) + (pg8::bf_hi(a.y) + pg8::bf_hi(b.y));
;                             ss += (v[q].x * v[q].x + v[q].y * v[q].y) + (v[q].z * v[q].z + v[q].w * v[q].w); }
;                         ss = wave_sum(ss, ln);
;                         GAS v2u* o8 = (GAS v2u*)(ub + (size_t)mr * D) + ln;
; #pragma unroll
;                         for (int q = 0; q < 4; ++q) { v2u w; w.x = pg8::pk_f16(v[q].x, v[q].y); w.y = pg8::pk_f16(v[q].z, v[q].w); o8[64 * q] = w; }
;                         if (ln < 16) ((float*)(ws + WS_TBL + T_SSP))[(size_t)mr * 16 + ln] = (ln == 0) ? ss : 0.f; }
	v_pk_add_f32 v[40:41], v[40:41], v[44:45]
	v_lshlrev_b32_e32 v44, 16, v36
	v_cvt_pk_f16_f32 v39, v40, v41
	global_store_dwordx2 v[18:19], v[38:39], off offset:1024
	v_cvt_f32_f16_sdwa v39, v32 dst_sel:DWORD dst_unused:UNUSED_PAD src0_sel:WORD_1
	v_cvt_f32_f16_e32 v38, v32
	v_pk_mul_f32 v[42:43], v[40:41], v[40:41]
	v_lshlrev_b32_e32 v40, 16, v34
	v_and_b32_e32 v41, 0xffff0000, v34
	v_and_b32_e32 v45, 0xffff0000, v36
	v_pk_add_f32 v[40:41], v[40:41], v[44:45]
	v_lshlrev_b32_e32 v32, 16, v35
	v_pk_add_f32 v[38:39], v[40:41], v[38:39]
	v_lshlrev_b32_e32 v36, 16, v37
	v_pk_mul_f32 v[40:41], v[38:39], v[38:39]
	v_cvt_pk_f16_f32 v34, v38, v39
	v_cvt_f32_f16_sdwa v39, v33 dst_sel:DWORD dst_unused:UNUSED_PAD src0_sel:WORD_1
	v_cvt_f32_f16_e32 v38, v33
	v_and_b32_e32 v33, 0xffff0000, v35
	v_and_b32_e32 v37, 0xffff0000, v37
	v_pk_add_f32 v[32:33], v[32:33], v[36:37]
	v_add_f32_e32 v35, v48, v49
	v_pk_add_f32 v[36:37], v[32:33], v[38:39]
	v_add_f32_e32 v38, v52, v53
	v_add_f32_e32 v35, v35, v38
	v_add_f32_e32 v38, v54, v55
	v_add_f32_e32 v39, v58, v59
	v_add_f32_e32 v38, v38, v39
	v_pk_mul_f32 v[32:33], v[36:37], v[36:37]
	v_add_f32_e32 v35, v38, v35
	v_add_f32_e32 v38, v42, v43
	v_add_f32_e32 v39, v46, v47
	v_add_f32_e32 v38, v38, v39
	v_add_f32_e32 v32, v32, v33
	v_add_f32_e32 v33, v40, v41
	v_add_f32_e32 v35, v35, v38
	v_add_f32_e32 v32, v32, v33
	v_add_f32_e32 v32, v35, v32
	ds_bpermute_b32 v33, v111, v32
	v_cvt_pk_f16_f32 v35, v36, v37
	global_store_dwordx2 v[18:19], v[34:35], off offset:1536
	s_waitcnt lgkmcnt(0)
	v_add_f32_e32 v32, v32, v33
	ds_bpermute_b32 v33, v112, v32
	s_waitcnt lgkmcnt(0)
	v_add_f32_e32 v32, v32, v33
	ds_bpermute_b32 v33, v113, v32
	s_waitcnt lgkmcnt(0)
	v_add_f32_e32 v32, v32, v33
	ds_bpermute_b32 v33, v114, v32
	s_waitcnt lgkmcnt(0)
	v_add_f32_e32 v32, v32, v33
	ds_bpermute_b32 v33, v115, v32
	s_waitcnt lgkmcnt(0)
	v_add_f32_e32 v32, v32, v33
	ds_bpermute_b32 v33, v116, v32
	s_and_saveexec_b64 s[0:1], vcc
	s_cbranch_execz .LBB0_1196
	s_waitcnt lgkmcnt(0)
	v_add_f32_e32 v32, v32, v33
	s_lshl_b64 s[8:9], s[8:9], 6
	v_lshl_add_u64 v[18:19], v[0:1], 0, s[8:9]
	v_cndmask_b32_e64 v32, 0, v32, s[2:3]
	global_store_dword v[18:19], v32, off
.LBB0_1196:
	s_or_b64 exec, exec, s[0:1]
	v_lshlrev_b32_e32 v32, 16, v28
	s_waitcnt lgkmcnt(0)
	v_and_b32_e32 v33, 0xffff0000, v28
	v_lshlrev_b32_e32 v34, 16, v26
	v_and_b32_e32 v35, 0xffff0000, v26
	v_cvt_f32_f16_sdwa v19, v30 dst_sel:DWORD dst_unused:UNUSED_PAD src0_sel:WORD_1
	v_cvt_f32_f16_e32 v18, v30
	v_pk_add_f32 v[32:33], v[32:33], v[34:35]
	v_cvt_f32_f16_sdwa v35, v31 dst_sel:DWORD dst_unused:UNUSED_PAD src0_sel:WORD_1
	v_cvt_f32_f16_e32 v34, v31
	v_lshlrev_b32_e32 v28, 16, v29
	v_and_b32_e32 v29, 0xffff0000, v29
	v_lshlrev_b32_e32 v26, 16, v27
	v_and_b32_e32 v27, 0xffff0000, v27
	v_pk_add_f32 v[26:27], v[28:29], v[26:27]
	v_pk_add_f32 v[18:19], v[32:33], v[18:19]
	v_pk_add_f32 v[26:27], v[26:27], v[34:35]
	v_pk_mul_f32 v[32:33], v[18:19], v[18:19]
	v_cvt_pk_f16_f32 v18, v18, v19
	v_pk_mul_f32 v[28:29], v[26:27], v[26:27]
	v_cvt_pk_f16_f32 v19, v26, v27
	v_lshlrev_b32_e32 v26, 16, v22
	v_and_b32_e32 v27, 0xffff0000, v22
	v_lshlrev_b32_e32 v30, 16, v20
	v_and_b32_e32 v31, 0xffff0000, v20
	global_store_dwordx2 v[4:5], v[18:19], off
	v_cvt_f32_f16_sdwa v19, v24 dst_sel:DWORD dst_unused:UNUSED_PAD src0_sel:WORD_1
	v_cvt_f32_f16_e32 v18, v24
	v_pk_add_f32 v[26:27], v[26:27], v[30:31]
	v_cvt_f32_f16_sdwa v31, v25 dst_sel:DWORD dst_unused:UNUSED_PAD src0_sel:WORD_1
	v_cvt_f32_f16_e32 v30, v25
	v_lshlrev_b32_e32 v22, 16, v23
	v_and_b32_e32 v23, 0xffff0000, v23
	v_lshlrev_b32_e32 v20, 16, v21
	v_and_b32_e32 v21, 0xffff0000, v21
	v_pk_add_f32 v[20:21], v[22:23], v[20:21]
	v_pk_add_f32 v[18:19], v[26:27], v[18:19]
	v_pk_add_f32 v[20:21], v[20:21], v[30:31]
	v_pk_mul_f32 v[26:27], v[18:19], v[18:19]
	v_cvt_pk_f16_f32 v18, v18, v19
	v_cvt_pk_f16_f32 v19, v20, v21
	global_store_dwordx2 v[4:5], v[18:19], off offset:512
	v_cvt_f32_f16_sdwa v19, v16 dst_sel:DWORD dst_unused:UNUSED_PAD src0_sel:WORD_1
	v_cvt_f32_f16_e32 v18, v16
	v_pk_mul_f32 v[22:23], v[20:21], v[20:21]
	v_lshlrev_b32_e32 v20, 16, v14
	v_and_b32_e32 v21, 0xffff0000, v14
	v_lshlrev_b32_e32 v24, 16, v12
	v_and_b32_e32 v25, 0xffff0000, v12
	v_pk_add_f32 v[20:21], v[20:21], v[24:25]
	v_lshlrev_b32_e32 v14, 16, v15
	v_pk_add_f32 v[18:19], v[20:21], v[18:19]
	v_and_b32_e32 v15, 0xffff0000, v15
	v_pk_mul_f32 v[20:21], v[18:19], v[18:19]
	v_cvt_pk_f16_f32 v12, v18, v19
	v_cvt_f32_f16_sdwa v19, v17 dst_sel:DWORD dst_unused:UNUSED_PAD src0_sel:WORD_1
	v_cvt_f32_f16_e32 v18, v17
	v_lshlrev_b32_e32 v16, 16, v13
	v_and_b32_e32 v17, 0xffff0000, v13
	v_pk_add_f32 v[14:15], v[14:15], v[16:17]
	s_nop 0
	v_pk_add_f32 v[14:15], v[14:15], v[18:19]
	v_lshlrev_b32_e32 v18, 16, v10
	v_cvt_pk_f16_f32 v13, v14, v15
	global_store_dwordx2 v[4:5], v[12:13], off offset:1024
	v_cvt_f32_f16_sdwa v13, v6 dst_sel:DWORD dst_unused:UNUSED_PAD src0_sel:WORD_1
	v_cvt_f32_f16_e32 v12, v6
	v_pk_mul_f32 v[16:17], v[14:15], v[14:15]
	v_lshlrev_b32_e32 v14, 16, v8
	v_and_b32_e32 v15, 0xffff0000, v8
	v_and_b32_e32 v19, 0xffff0000, v10
	v_pk_add_f32 v[14:15], v[14:15], v[18:19]
	v_lshlrev_b32_e32 v6, 16, v9
	v_pk_add_f32 v[12:13], v[14:15], v[12:13]
	v_lshlrev_b32_e32 v10, 16, v11
	v_pk_mul_f32 v[14:15], v[12:13], v[12:13]
	v_cvt_pk_f16_f32 v8, v12, v13
	v_cvt_f32_f16_sdwa v13, v7 dst_sel:DWORD dst_unused:UNUSED_PAD src0_sel:WORD_1
	v_cvt_f32_f16_e32 v12, v7
	v_and_b32_e32 v7, 0xffff0000, v9
	v_and_b32_e32 v11, 0xffff0000, v11
	v_pk_add_f32 v[6:7], v[6:7], v[10:11]
	v_add_f32_e32 v9, v22, v23
	v_pk_add_f32 v[10:11], v[6:7], v[12:13]
	v_add_f32_e32 v12, v26, v27
	v_add_f32_e32 v9, v9, v12
	v_add_f32_e32 v12, v28, v29
	v_add_f32_e32 v13, v32, v33
	v_add_f32_e32 v12, v12, v13
	v_pk_mul_f32 v[6:7], v[10:11], v[10:11]
	v_add_f32_e32 v9, v12, v9
	v_add_f32_e32 v12, v16, v17
	v_add_f32_e32 v13, v20, v21
	v_add_f32_e32 v12, v12, v13
	v_add_f32_e32 v6, v6, v7
	v_add_f32_e32 v7, v14, v15
	v_add_f32_e32 v9, v9, v12
	v_add_f32_e32 v6, v6, v7
	v_add_f32_e32 v6, v9, v6
	ds_bpermute_b32 v7, v111, v6
	v_cvt_pk_f16_f32 v9, v10, v11
	global_store_dwordx2 v[4:5], v[8:9], off offset:1536
	s_waitcnt lgkmcnt(0)
	v_add_f32_e32 v6, v6, v7
	ds_bpermute_b32 v7, v112, v6
	s_waitcnt lgkmcnt(0)
	v_add_f32_e32 v6, v6, v7
	ds_bpermute_b32 v7, v113, v6
	s_waitcnt lgkmcnt(0)
	v_add_f32_e32 v6, v6, v7
	ds_bpermute_b32 v7, v114, v6
	s_waitcnt lgkmcnt(0)
	v_add_f32_e32 v6, v6, v7
	ds_bpermute_b32 v7, v115, v6
	s_waitcnt lgkmcnt(0)
	v_add_f32_e32 v6, v6, v7
	ds_bpermute_b32 v7, v116, v6
	s_and_saveexec_b64 s[0:1], vcc
	s_cbranch_execz .LBB0_1189
	s_waitcnt lgkmcnt(0)
	v_add_f32_e32 v6, v6, v7
	s_lshl_b64 s[6:7], s[6:7], 6
	v_lshl_add_u64 v[4:5], v[0:1], 0, s[6:7]
	v_cndmask_b32_e64 v6, 0, v6, s[2:3]
	global_store_dword v[4:5], v6, off
	s_branch .LBB0_1189

; __device__ __forceinline__ float f16_lo(unsigned u) { return (float)__builtin_bit_cast(h16x2, u)[0]; }
; __device__ __forceinline__ float f16_hi(unsigned u) { return (float)__builtin_bit_cast(h16x2, u)[1]; }
; #define GAS __attribute__((address_space(1)))
; #define OPQ_LANE() int z_ = 0; asm volatile("" : "+v"(z_)); const int ln = (int)__builtin_amdgcn_mbcnt_hi(~0u, __builtin_amdgcn_mbcnt_lo(~0u, (unsigned)z_)); const int tidv = F.wave * 64 + ln; (void)tidv; int bix = blockIdx.x; asm volatile("" : "+s"(bix)); (void)bix
; __global__ void __launch_bounds__(NWAVES * 64, 2) mk_fwd(Args args) {
;     ...
;     if (IN(PH_FINAL)) {
;         WSPTRS();
;         OPQ_LANE();
;         { int m = gw; asm volatile("" : "+s"(m)); const GAS f32x4* gr = (const GAS f32x4*)ap->in[22] + ln;
;           for (; m < M; m += 2 * NGW) { f32x4 v[2][4]; float ss[2] = {0.f, 0.f};
; #pragma unroll
;               for (int r = 0; r < 2; ++r) { const GAS v2u* xr = (const GAS v2u*)(hx + (size_t)(m + r * NGW) * D) + ln;
; #pragma unroll
;                   for (int q = 0; q < 4; ++q) { const v2u hv = xr[64 * q]; v[r][q] = (f32x4){pg8::f16_lo(hv.x), pg8::f16_hi(hv.x), pg8::f16_lo(hv.y), pg8::f16_hi(hv.y)}; } }
; #pragma unroll
;               for (int r = 0; r < 2; ++r) {
; #pragma unroll
;                   for (int q = 0; q < 4; ++q) ss[r] += (v[r][q].x * v[r][q].x + v[r][q].y * v[r][q].y) + (v[r][q].z * v[r][q].z + v[r][q].w * v[r][q].w);
.LBB0_1355:
	s_cmpk_lt_i32 s72, 0x42
	s_cselect_b64 s[0:1], -1, 0
	s_cmpk_gt_i32 s73, 0x41
	s_cselect_b64 s[2:3], -1, 0
	s_and_b64 s[0:1], s[0:1], s[2:3]
	s_and_b64 vcc, exec, s[0:1]
	s_cbranch_vccz .LBB0_1359
	v_mov_b32_e32 v0, 0
	v_readlane_b32 s0, v254, 2
	s_cmpk_gt_i32 s60, 0x3fff
	s_cbranch_scc1 .LBB0_1359
	v_mov_b64_e32 v[2:3], s[66:67]
	global_load_dwordx2 v[8:9], v[2:3], off offset:176
	v_mbcnt_lo_u32_b32 v3, -1, v0
	v_mbcnt_hi_u32_b32 v16, -1, v3
	s_add_u32 s1, s80, 0x600000
	v_ashrrev_i32_e32 v17, 31, v16
	v_lshlrev_b32_e32 v4, 2, v16
	s_waitcnt lgkmcnt(0)
	v_mov_b64_e32 v[0:1], s[66:67]
	s_mov_b32 s0, 0x3a800000
	v_mov_b32_e32 v2, 0x358637bd
	s_addc_u32 s4, s81, 0
	s_lshl_b32 s5, s59, 4
	v_xor_b32_e32 v3, 4, v4
	v_xor_b32_e32 v10, 8, v4
	v_xor_b32_e32 v11, 16, v4
	v_xor_b32_e32 v12, 32, v4
	v_xor_b32_e32 v13, 64, v4
	v_xor_b32_e32 v14, 0x80, v4
	v_lshlrev_b64 v[4:5], 3, v[16:17]
	v_lshlrev_b64 v[6:7], 4, v[16:17]
	s_mov_b32 s6, 0x800000
	s_waitcnt vmcnt(0)
	v_lshl_add_u64 v[8:9], v[16:17], 4, v[8:9]
.LBB0_1358:
	s_ashr_i32 s61, s60, 31
	s_lshl_b64 s[2:3], s[60:61], 11
	s_add_u32 s2, s1, s2
	s_addc_u32 s3, s4, s3
	v_lshl_add_u64 v[16:17], s[2:3], 0, v[4:5]
	global_load_dwordx2 v[20:21], v[16:17], off
	global_load_dwordx2 v[22:23], v[16:17], off offset:512
	global_load_dwordx2 v[24:25], v[16:17], off offset:1024
	s_add_i32 s2, s54, s60
	global_load_dwordx2 v[26:27], v[16:17], off offset:1536
	s_ashr_i32 s3, s2, 31
	s_lshl_b64 s[8:9], s[2:3], 11
	s_add_u32 s8, s1, s8
	s_addc_u32 s9, s4, s9
	v_lshl_add_u64 v[28:29], s[8:9], 0, v[4:5]
	global_load_dwordx2 v[30:31], v[28:29], off
	global_load_dwordx2 v[32:33], v[28:29], off offset:512
	global_load_dwordx2 v[34:35], v[28:29], off offset:1024
	global_load_dwordx2 v[36:37], v[28:29], off offset:1536
	global_load_dwordx2 v[38:39], v[0:1], off offset:184
	global_load_dwordx4 v[16:19], v[8:9], off
	s_lshl_b64 s[8:9], s[60:61], 12
	s_lshl_b64 s[2:3], s[2:3], 12
	s_add_i32 s60, s60, s5
	s_cmpk_lt_i32 s60, 0x4000
	s_waitcnt vmcnt(0)
	v_cvt_f32_f16_e32 v28, v20
	v_cvt_f32_f16_sdwa v29, v20 dst_sel:DWORD dst_unused:UNUSED_PAD src0_sel:WORD_1
	v_cvt_f32_f16_e32 v20, v21
	v_cvt_f32_f16_sdwa v21, v21 dst_sel:DWORD dst_unused:UNUSED_PAD src0_sel:WORD_1
	v_cvt_f32_f16_e32 v40, v22
	v_cvt_f32_f16_sdwa v41, v22 dst_sel:DWORD dst_unused:UNUSED_PAD src0_sel:WORD_1
	v_cvt_f32_f16_e32 v22, v23
	v_cvt_f32_f16_sdwa v23, v23 dst_sel:DWORD dst_unused:UNUSED_PAD src0_sel:WORD_1
	v_cvt_f32_f16_e32 v42, v24
	v_cvt_f32_f16_sdwa v43, v24 dst_sel:DWORD dst_unused:UNUSED_PAD src0_sel:WORD_1
	v_cvt_f32_f16_e32 v24, v25
	v_cvt_f32_f16_sdwa v25, v25 dst_sel:DWORD dst_unused:UNUSED_PAD src0_sel:WORD_1
	v_cvt_f32_f16_e32 v44, v26
	v_cvt_f32_f16_sdwa v45, v26 dst_sel:DWORD dst_unused:UNUSED_PAD src0_sel:WORD_1
	v_cvt_f32_f16_e32 v26, v27
	v_cvt_f32_f16_sdwa v27, v27 dst_sel:DWORD dst_unused:UNUSED_PAD src0_sel:WORD_1
	v_cvt_f32_f16_e32 v46, v30
	v_cvt_f32_f16_sdwa v47, v30 dst_sel:DWORD dst_unused:UNUSED_PAD src0_sel:WORD_1
	v_cvt_f32_f16_e32 v30, v31
	v_cvt_f32_f16_sdwa v31, v31 dst_sel:DWORD dst_unused:UNUSED_PAD src0_sel:WORD_1
	v_cvt_f32_f16_e32 v48, v32
	v_cvt_f32_f16_sdwa v49, v32 dst_sel:DWORD dst_unused:UNUSED_PAD src0_sel:WORD_1
	v_cvt_f32_f16_e32 v32, v33
	v_cvt_f32_f16_sdwa v33, v33 dst_sel:DWORD dst_unused:UNUSED_PAD src0_sel:WORD_1
	v_mov_b32_e32 v56, v29
	v_mov_b32_e32 v57, v21
	v_mov_b32_e32 v60, v41
	v_mov_b32_e32 v61, v23
	v_mov_b32_e32 v54, v28
	v_mov_b32_e32 v55, v20
	v_mov_b32_e32 v58, v40
	v_mov_b32_e32 v59, v22
	v_mul_f32_e32 v62, v43, v43
	v_mul_f32_e32 v64, v25, v25
	v_pk_mul_f32 v[56:57], v[56:57], v[56:57]
	v_pk_mul_f32 v[60:61], v[60:61], v[60:61]
	v_cvt_f32_f16_e32 v50, v34
	v_cvt_f32_f16_sdwa v51, v34 dst_sel:DWORD dst_unused:UNUSED_PAD src0_sel:WORD_1
	v_cvt_f32_f16_e32 v34, v35
	v_cvt_f32_f16_sdwa v35, v35 dst_sel:DWORD dst_unused:UNUSED_PAD src0_sel:WORD_1
	v_pk_mul_f32 v[68:69], v[26:27], v[26:27]
	v_pk_fma_f32 v[62:63], v[42:43], v[42:43], v[62:63] op_sel_hi:[1,1,0]
	v_pk_fma_f32 v[64:65], v[24:25], v[24:25], v[64:65] op_sel_hi:[1,1,0]
	v_pk_fma_f32 v[54:55], v[54:55], v[54:55], v[56:57]
	v_pk_fma_f32 v[56:57], v[58:59], v[58:59], v[60:61]
	v_cvt_f32_f16_e32 v52, v36
	v_cvt_f32_f16_sdwa v53, v36 dst_sel:DWORD dst_unused:UNUSED_PAD src0_sel:WORD_1
	v_cvt_f32_f16_e32 v36, v37
	v_cvt_f32_f16_sdwa v37, v37 dst_sel:DWORD dst_unused:UNUSED_PAD src0_sel:WORD_1
	v_pk_mul_f32 v[66:67], v[44:45], v[44:45]
	v_mov_b32_e32 v63, v68
	v_mov_b32_e32 v65, v69
	v_pk_add_f32 v[54:55], v[54:55], v[54:55] op_sel:[0,1] op_sel_hi:[1,0]
	v_pk_add_f32 v[56:57], v[56:57], v[56:57] op_sel:[0,1] op_sel_hi:[1,0]
	v_pk_add_f32 v[58:59], v[62:63], v[64:65]
	v_mov_b32_e32 v55, v66
	v_mov_b32_e32 v57, v67
	v_mov_b32_e32 v62, v47
	v_mov_b32_e32 v63, v31
	v_mov_b32_e32 v66, v49
	v_mov_b32_e32 v67, v33
	v_mov_b32_e32 v60, v46
	v_mov_b32_e32 v61, v30
	v_mov_b32_e32 v64, v48
	v_mov_b32_e32 v65, v32
	v_pk_add_f32 v[54:55], v[54:55], v[56:57]
	v_pk_mul_f32 v[56:57], v[62:63], v[62:63]
	v_pk_mul_f32 v[62:63], v[66:67], v[66:67]
	v_mul_f32_e32 v68, v51, v51
	v_mul_f32_e32 v70, v35, v35
	v_pk_add_f32 v[54:55], v[54:55], v[58:59]
	v_pk_fma_f32 v[56:57], v[60:61], v[60:61], v[56:57]
	v_pk_fma_f32 v[58:59], v[64:65], v[64:65], v[62:63]
	v_pk_fma_f32 v[66:67], v[50:51], v[50:51], v[68:69] op_sel_hi:[1,1,0]
	v_pk_add_f32 v[56:57], v[56:57], v[56:57] op_sel:[0,1] op_sel_hi:[1,0]
	v_pk_add_f32 v[58:59], v[58:59], v[58:59] op_sel:[0,1] op_sel_hi:[1,0]
	v_pk_fma_f32 v[60:61], v[34:35], v[34:35], v[70:71] op_sel_hi:[1,1,0]
	v_pk_mul_f32 v[62:63], v[52:53], v[52:53]
	v_pk_mul_f32 v[64:65], v[36:37], v[36:37]
	v_mov_b32_e32 v57, v62
	v_mov_b32_e32 v59, v63
	v_mov_b32_e32 v67, v64
	v_mov_b32_e32 v61, v65
	v_pk_add_f32 v[56:57], v[56:57], v[58:59]
	v_pk_add_f32 v[58:59], v[66:67], v[60:61]
	s_waitcnt lgkmcnt(0)
; #define GAS __attribute__((address_space(1)))
; __global__ void __launch_bounds__(NWAVES * 64, 2) mk_fwd(Args args) {
;     ...
; #pragma unroll
;               for (int r = 0; r < 2; ++r) {
; #pragma unroll
;                   for (int q = 0; q < 4; ++q) ss[r] += (v[r][q].x * v[r][q].x + v[r][q].y * v[r][q].y) + (v[r][q].z * v[r][q].z + v[r][q].w * v[r][q].w);
;                   const float rstd = rsqrtf(wave_sum(ss[r], ln) * (1.f / D) + EPS); GAS f32x4* o = (GAS f32x4*)(ap->out + (size_t)(m + r * NGW) * D) + ln;
; #pragma unroll
;                   for (int q = 0; q < 4; ++q) o[64 * q] = v[r][q] * rstd * gr[64 * q]; } } }
	v_lshl_add_u64 v[38:39], v[38:39], 0, s[8:9]
	v_pk_add_f32 v[56:57], v[56:57], v[58:59]
	v_mov_b32_e32 v59, v54
	v_mov_b32_e32 v58, v56
	v_mov_b32_e32 v54, v57
	v_pk_add_f32 v[54:55], v[58:59], v[54:55]
	ds_bpermute_b32 v57, v3, v55
	ds_bpermute_b32 v56, v3, v54
	v_lshl_add_u64 v[38:39], v[38:39], 0, v[6:7]
	s_waitcnt lgkmcnt(0)
	v_pk_add_f32 v[54:55], v[54:55], v[56:57]
	ds_bpermute_b32 v57, v10, v55
	ds_bpermute_b32 v56, v10, v54
	s_waitcnt lgkmcnt(0)
	v_pk_add_f32 v[54:55], v[54:55], v[56:57]
	ds_bpermute_b32 v57, v11, v55
	ds_bpermute_b32 v56, v11, v54
	s_waitcnt lgkmcnt(0)
	v_pk_add_f32 v[54:55], v[54:55], v[56:57]
	ds_bpermute_b32 v57, v12, v55
	ds_bpermute_b32 v56, v12, v54
	s_waitcnt lgkmcnt(0)
	v_pk_add_f32 v[54:55], v[54:55], v[56:57]
	ds_bpermute_b32 v57, v13, v55
	ds_bpermute_b32 v56, v13, v54
	s_waitcnt lgkmcnt(0)
	v_pk_add_f32 v[54:55], v[54:55], v[56:57]
	ds_bpermute_b32 v57, v14, v55
	ds_bpermute_b32 v56, v14, v54
	s_waitcnt lgkmcnt(0)
	v_pk_add_f32 v[54:55], v[54:55], v[56:57]
	s_nop 0
	v_pk_fma_f32 v[54:55], v[54:55], s[0:1], v[2:3] op_sel_hi:[1,0,0]
	s_nop 0
	v_mul_f32_e32 v15, 0x4b800000, v55
	v_cmp_gt_f32_e32 vcc, s6, v55
	s_nop 1
	v_cndmask_b32_e32 v15, v55, v15, vcc
	v_rsq_f32_e32 v15, v15
	s_nop 0
	v_mul_f32_e32 v55, 0x45800000, v15
	v_cndmask_b32_e32 v56, v15, v55, vcc
	v_pk_mul_f32 v[28:29], v[56:57], v[28:29] op_sel_hi:[0,1]
	v_pk_mul_f32 v[20:21], v[56:57], v[20:21] op_sel_hi:[0,1]
	v_pk_mul_f32 v[18:19], v[20:21], v[18:19]
	v_pk_mul_f32 v[16:17], v[28:29], v[16:17]
	global_store_dwordx4 v[38:39], v[16:19], off
	global_load_dwordx4 v[16:19], v[8:9], off offset:1024
	v_pk_mul_f32 v[20:21], v[56:57], v[22:23] op_sel_hi:[0,1]
	v_pk_mul_f32 v[22:23], v[56:57], v[40:41] op_sel_hi:[0,1]
	v_mul_f32_e32 v15, 0x4b800000, v54
	v_cmp_gt_f32_e32 vcc, s6, v54
	s_waitcnt vmcnt(0)
	v_pk_mul_f32 v[16:17], v[22:23], v[16:17]
	v_pk_mul_f32 v[18:19], v[20:21], v[18:19]
	global_store_dwordx4 v[38:39], v[16:19], off offset:1024
	global_load_dwordx4 v[16:19], v[8:9], off offset:2048
	v_pk_mul_f32 v[20:21], v[56:57], v[24:25] op_sel_hi:[0,1]
	v_pk_mul_f32 v[22:23], v[56:57], v[42:43] op_sel_hi:[0,1]
	v_cndmask_b32_e32 v15, v54, v15, vcc
	v_rsq_f32_e32 v15, v15
	s_waitcnt vmcnt(0)
	v_pk_mul_f32 v[16:17], v[22:23], v[16:17]
	v_pk_mul_f32 v[18:19], v[20:21], v[18:19]
	global_store_dwordx4 v[38:39], v[16:19], off offset:2048
	global_load_dwordx4 v[16:19], v[8:9], off offset:3072
	v_pk_mul_f32 v[20:21], v[56:57], v[26:27] op_sel_hi:[0,1]
	v_pk_mul_f32 v[22:23], v[56:57], v[44:45] op_sel_hi:[0,1]
	s_waitcnt vmcnt(0)
	v_pk_mul_f32 v[16:17], v[22:23], v[16:17]
	v_pk_mul_f32 v[18:19], v[20:21], v[18:19]
	global_store_dwordx4 v[38:39], v[16:19], off offset:3072
	global_load_dwordx2 v[20:21], v[0:1], off offset:184
	s_nop 0
	global_load_dwordx4 v[16:19], v[8:9], off
	v_mul_f32_e32 v22, 0x45800000, v15
	v_cndmask_b32_e32 v22, v15, v22, vcc
	v_pk_mul_f32 v[24:25], v[22:23], v[30:31] op_sel_hi:[0,1]
	v_pk_mul_f32 v[26:27], v[22:23], v[46:47] op_sel_hi:[0,1]
	s_waitcnt vmcnt(0) lgkmcnt(0)
	v_lshl_add_u64 v[20:21], v[20:21], 0, s[2:3]
	v_pk_mul_f32 v[16:17], v[26:27], v[16:17]
	v_pk_mul_f32 v[18:19], v[24:25], v[18:19]
	v_lshl_add_u64 v[20:21], v[20:21], 0, v[6:7]
	global_store_dwordx4 v[20:21], v[16:19], off
	global_load_dwordx4 v[16:19], v[8:9], off offset:1024
	v_pk_mul_f32 v[24:25], v[22:23], v[32:33] op_sel_hi:[0,1]
	v_pk_mul_f32 v[26:27], v[22:23], v[48:49] op_sel_hi:[0,1]
	s_waitcnt vmcnt(0)
	v_pk_mul_f32 v[16:17], v[26:27], v[16:17]
	v_pk_mul_f32 v[18:19], v[24:25], v[18:19]
	global_store_dwordx4 v[20:21], v[16:19], off offset:1024
	global_load_dwordx4 v[16:19], v[8:9], off offset:2048
	v_pk_mul_f32 v[24:25], v[22:23], v[34:35] op_sel_hi:[0,1]
	v_pk_mul_f32 v[26:27], v[22:23], v[50:51] op_sel_hi:[0,1]
	s_waitcnt vmcnt(0)
	v_pk_mul_f32 v[16:17], v[26:27], v[16:17]
	v_pk_mul_f32 v[18:19], v[24:25], v[18:19]
	global_store_dwordx4 v[20:21], v[16:19], off offset:2048
	global_load_dwordx4 v[16:19], v[8:9], off offset:3072
	v_pk_mul_f32 v[24:25], v[22:23], v[36:37] op_sel_hi:[0,1]
	v_pk_mul_f32 v[22:23], v[22:23], v[52:53] op_sel_hi:[0,1]
	s_waitcnt vmcnt(0)
	v_pk_mul_f32 v[16:17], v[22:23], v[16:17]
	v_pk_mul_f32 v[18:19], v[24:25], v[18:19]
	global_store_dwordx4 v[20:21], v[16:19], off offset:3072
	s_cbranch_scc1 .LBB0_1358
